# baseline (speedup 1.0000x reference)
_Z14k1_stats_graphPKfS0_S0_PdPfPiPyPtS2_S3_:
	s_load_dwordx4 s[4:7], s[0:1], 0x0
	s_load_dwordx4 s[12:15], s[0:1], 0x30
	s_load_dwordx4 s[8:11], s[0:1], 0x18
	s_load_dwordx4 s[16:19], s[0:1], 0x40
	s_load_dwordx2 s[20:21], s[0:1], 0x28
	v_and_b32_e32 v1, 63, v0
	v_lshrrev_b32_e32 v2, 6, v0
	v_lshlrev_b32_e32 v12, 4, v1
	v_add_u32_e32 v13, 0x1000, v12
	v_mov_b32_e32 v15, 0xff800000
	v_readfirstlane_b32 s3, v2
	s_lshl_b32 s24, s2, 2
	s_add_u32 s24, s24, s3
	s_lshr_b32 s25, s24, 9
	s_and_b32 s26, s24, 0x1ff
	s_lshl_b32 s27, s24, 4
	s_lshl_b32 s32, s25, 9
	s_lshl_b32 s33, s3, 7
	s_add_u32 s32, s32, s33
	v_add_u32_e32 v3, s32, v1
	v_lshlrev_b32_e32 v3, 4, v3
	s_mul_i32 s34, s24, 0x641
	s_and_b32 s35, s34, 3
	s_andn2_b32 s34, s34, 3
	s_lshl_b32 s34, s34, 2
	s_waitcnt lgkmcnt(0)
	s_load_dwordx4 s[28:31], s[4:5], s27
	global_load_dwordx4 v[4:7], v3, s[4:5]
	global_load_dwordx4 v[8:11], v3, s[4:5] offset:1024
	s_add_u32 s36, s6, s34
	s_addc_u32 s37, s7, 0
	global_load_dwordx4 v[16:19], v12, s[36:37] offset:0 nt
	global_load_dwordx4 v[20:23], v12, s[36:37] offset:1024 nt
	global_load_dwordx4 v[24:27], v12, s[36:37] offset:2048 nt
	global_load_dwordx4 v[28:31], v12, s[36:37] offset:3072 nt
	global_load_dwordx4 v[32:35], v13, s[36:37] offset:0 nt
	global_load_dwordx4 v[36:39], v13, s[36:37] offset:1024 nt
	v_mov_b32_e32 v40, v15
	v_mov_b32_e32 v41, v15
	v_mov_b32_e32 v42, v15
	v_mov_b32_e32 v43, v15
	s_mov_b64 exec, 0x1ffff
	global_load_dwordx4 v[40:43], v13, s[36:37] offset:2048 nt
	s_mov_b64 exec, -1
	s_lshl_b32 s33, s3, 11
	v_add_u32_e32 v14, s33, v12
	s_mov_b32 s39, 0xb8d1b717
	v_mov_b32_e32 v60, 0x7f800000
	s_waitcnt vmcnt(7)
	ds_write_b128 v14, v[4:7]
	ds_write_b128 v14, v[8:11] offset:1024
	s_waitcnt lgkmcnt(0)
	v_mov_b32_e32 v52, s28
	v_mov_b32_e32 v53, s29
	v_sub_f32_e32 v52, s30, v52
	v_sub_f32_e32 v53, s31, v53
	v_mul_f32_e32 v52, v52, v53
	s_barrier
	v_readfirstlane_b32 s38, v52
	ds_read_b128 v[4:7], v12 offset:0
	ds_read_b128 v[8:11], v12 offset:1024
	ds_read_b128 v[44:47], v12 offset:2048
	ds_read_b128 v[48:51], v12 offset:3072
	s_waitcnt lgkmcnt(3)
	v_sub_f32_e32 v52, v6, v4
	v_sub_f32_e32 v53, v7, v5
	v_min_f32_e32 v54, s30, v6
	v_max_f32_e32 v55, s28, v4
	v_min_f32_e32 v56, s31, v7
	v_max_f32_e32 v57, s29, v5
	v_mul_f32_e32 v52, v52, v53
	v_sub_f32_e32 v54, v54, v55
	v_sub_f32_e32 v56, v56, v57
	v_max_f32_e32 v54, 0, v54
	v_max_f32_e32 v56, 0, v56
	v_add_f32_e32 v52, s38, v52
	v_mul_f32_e32 v54, v54, v56
	v_sub_f32_e32 v52, v52, v54
	v_fma_f32 v55, v52, -0.5, v54
	v_fma_f32 v53, v52, s39, |v55|
	v_cmp_gt_f32_e64 s[40:41], v55, 0
	v_min_f32_e32 v60, v60, v53
	ds_read_b128 v[4:7], v12 offset:4096
	s_waitcnt lgkmcnt(3)
	v_sub_f32_e32 v52, v10, v8
	v_sub_f32_e32 v53, v11, v9
	v_min_f32_e32 v54, s30, v10
	v_max_f32_e32 v55, s28, v8
	v_min_f32_e32 v56, s31, v11
	v_max_f32_e32 v57, s29, v9
	v_mul_f32_e32 v52, v52, v53
	v_sub_f32_e32 v54, v54, v55
	v_sub_f32_e32 v56, v56, v57
	v_max_f32_e32 v54, 0, v54
	v_max_f32_e32 v56, 0, v56
	v_add_f32_e32 v52, s38, v52
	v_mul_f32_e32 v54, v54, v56
	v_sub_f32_e32 v52, v52, v54
	v_fma_f32 v55, v52, -0.5, v54
	v_fma_f32 v53, v52, s39, |v55|
	v_cmp_gt_f32_e64 s[42:43], v55, 0
	v_min_f32_e32 v60, v60, v53
	ds_read_b128 v[8:11], v12 offset:5120
	s_waitcnt lgkmcnt(3)
	v_sub_f32_e32 v52, v46, v44
	v_sub_f32_e32 v53, v47, v45
	v_min_f32_e32 v54, s30, v46
	v_max_f32_e32 v55, s28, v44
	v_min_f32_e32 v56, s31, v47
	v_max_f32_e32 v57, s29, v45
	v_mul_f32_e32 v52, v52, v53
	v_sub_f32_e32 v54, v54, v55
	v_sub_f32_e32 v56, v56, v57
	v_max_f32_e32 v54, 0, v54
	v_max_f32_e32 v56, 0, v56
	v_add_f32_e32 v52, s38, v52
	v_mul_f32_e32 v54, v54, v56
	v_sub_f32_e32 v52, v52, v54
	v_fma_f32 v55, v52, -0.5, v54
	v_fma_f32 v53, v52, s39, |v55|
	v_cmp_gt_f32_e64 s[44:45], v55, 0
	v_min_f32_e32 v60, v60, v53
	ds_read_b128 v[44:47], v12 offset:6144
	s_waitcnt lgkmcnt(3)
	v_sub_f32_e32 v52, v50, v48
	v_sub_f32_e32 v53, v51, v49
	v_min_f32_e32 v54, s30, v50
	v_max_f32_e32 v55, s28, v48
	v_min_f32_e32 v56, s31, v51
	v_max_f32_e32 v57, s29, v49
	v_mul_f32_e32 v52, v52, v53
	v_sub_f32_e32 v54, v54, v55
	v_sub_f32_e32 v56, v56, v57
	v_max_f32_e32 v54, 0, v54
	v_max_f32_e32 v56, 0, v56
	v_add_f32_e32 v52, s38, v52
	v_mul_f32_e32 v54, v54, v56
	v_sub_f32_e32 v52, v52, v54
	v_fma_f32 v55, v52, -0.5, v54
	v_fma_f32 v53, v52, s39, |v55|
	v_cmp_gt_f32_e64 s[46:47], v55, 0
	v_min_f32_e32 v60, v60, v53
	ds_read_b128 v[48:51], v12 offset:7168
	s_waitcnt lgkmcnt(3)
	v_sub_f32_e32 v52, v6, v4
	v_sub_f32_e32 v53, v7, v5
	v_min_f32_e32 v54, s30, v6
	v_max_f32_e32 v55, s28, v4
	v_min_f32_e32 v56, s31, v7
	v_max_f32_e32 v57, s29, v5
	v_mul_f32_e32 v52, v52, v53
	v_sub_f32_e32 v54, v54, v55
	v_sub_f32_e32 v56, v56, v57
	v_max_f32_e32 v54, 0, v54
	v_max_f32_e32 v56, 0, v56
	v_add_f32_e32 v52, s38, v52
	v_mul_f32_e32 v54, v54, v56
	v_sub_f32_e32 v52, v52, v54
	v_fma_f32 v55, v52, -0.5, v54
	v_fma_f32 v53, v52, s39, |v55|
	v_cmp_gt_f32_e64 s[48:49], v55, 0
	v_min_f32_e32 v60, v60, v53
	s_waitcnt lgkmcnt(2)
	v_sub_f32_e32 v52, v10, v8
	v_sub_f32_e32 v53, v11, v9
	v_min_f32_e32 v54, s30, v10
	v_max_f32_e32 v55, s28, v8
	v_min_f32_e32 v56, s31, v11
	v_max_f32_e32 v57, s29, v9
	v_mul_f32_e32 v52, v52, v53
	v_sub_f32_e32 v54, v54, v55
	v_sub_f32_e32 v56, v56, v57
	v_max_f32_e32 v54, 0, v54
	v_max_f32_e32 v56, 0, v56
	v_add_f32_e32 v52, s38, v52
	v_mul_f32_e32 v54, v54, v56
	v_sub_f32_e32 v52, v52, v54
	v_fma_f32 v55, v52, -0.5, v54
	v_fma_f32 v53, v52, s39, |v55|
	v_cmp_gt_f32_e64 s[50:51], v55, 0
	v_min_f32_e32 v60, v60, v53
	s_waitcnt lgkmcnt(1)
	v_sub_f32_e32 v52, v46, v44
	v_sub_f32_e32 v53, v47, v45
	v_min_f32_e32 v54, s30, v46
	v_max_f32_e32 v55, s28, v44
	v_min_f32_e32 v56, s31, v47
	v_max_f32_e32 v57, s29, v45
	v_mul_f32_e32 v52, v52, v53
	v_sub_f32_e32 v54, v54, v55
	v_sub_f32_e32 v56, v56, v57
	v_max_f32_e32 v54, 0, v54
	v_max_f32_e32 v56, 0, v56
	v_add_f32_e32 v52, s38, v52
	v_mul_f32_e32 v54, v54, v56
	v_sub_f32_e32 v52, v52, v54
	v_fma_f32 v55, v52, -0.5, v54
	v_fma_f32 v53, v52, s39, |v55|
	v_cmp_gt_f32_e64 s[52:53], v55, 0
	v_min_f32_e32 v60, v60, v53
	s_waitcnt lgkmcnt(0)
	v_sub_f32_e32 v52, v50, v48
	v_sub_f32_e32 v53, v51, v49
	v_min_f32_e32 v54, s30, v50
	v_max_f32_e32 v55, s28, v48
	v_min_f32_e32 v56, s31, v51
	v_max_f32_e32 v57, s29, v49
	v_mul_f32_e32 v52, v52, v53
	v_sub_f32_e32 v54, v54, v55
	v_sub_f32_e32 v56, v56, v57
	v_max_f32_e32 v54, 0, v54
	v_max_f32_e32 v56, 0, v56
	v_add_f32_e32 v52, s38, v52
	v_mul_f32_e32 v54, v54, v56
	v_sub_f32_e32 v52, v52, v54
	v_fma_f32 v55, v52, -0.5, v54
	v_fma_f32 v53, v52, s39, |v55|
	v_cmp_gt_f32_e64 s[54:55], v55, 0
	v_min_f32_e32 v60, v60, v53
	v_cmp_ge_f32_e32 vcc, 0, v60
	s_cbranch_vccnz .Lk1_rare

.Lk1_lse:
	s_mov_b32 s40, 0x652b82fe
	s_mov_b32 s41, 0x3ff71547
	s_mov_b32 s42, 0xfee00000
	s_mov_b32 s43, 0xbfe62e42
	s_mov_b32 s44, 0x35793c76
	s_mov_b32 s45, 0xbdea39ef
	s_mov_b32 s46, 0xb7789f5c
	s_mov_b32 s47, 0x3e927e4f
	s_mov_b32 s48, 0xa556c734
	s_mov_b32 s49, 0x3ec71de3
	s_mov_b32 s50, 0x1a01a01a
	s_mov_b32 s51, 0x3efa01a0
	s_mov_b32 s52, 0x1a01a01a
	s_mov_b32 s53, 0x3f2a01a0
	s_mov_b32 s54, 0x16c16c17
	s_mov_b32 s55, 0x3f56c16c
	s_mov_b32 s56, 0x11111111
	s_mov_b32 s57, 0x3f811111
	s_mov_b32 s58, 0x55555555
	s_mov_b32 s59, 0x3fa55555
	s_mov_b32 s60, 0x55555555
	s_mov_b32 s61, 0x3fc55555
	v_mov_b32_e32 v44, 0x67f544e4
	v_mov_b32_e32 v45, 0x3e5ae645
	v_cvt_f32_f64_e32 v52, v[6:7]
	v_log_f32_e32 v52, v52
	s_nop 0
	v_mul_f32_e32 v52, 0x3f317218, v52
	v_cvt_f64_f32_e32 v[8:9], v52
	v_mul_f64 v[10:11], v[8:9], -1.0
	v_mul_f64 v[46:47], v[10:11], s[40:41]
	v_rndne_f64_e32 v[46:47], v[46:47]
	v_fma_f64 v[10:11], v[46:47], s[42:43], v[10:11]
	v_fma_f64 v[10:11], v[46:47], s[44:45], v[10:11]
	v_fma_f64 v[48:49], v[44:45], v[10:11], s[46:47]
	v_fma_f64 v[48:49], v[48:49], v[10:11], s[48:49]
	v_fma_f64 v[48:49], v[48:49], v[10:11], s[50:51]
	v_fma_f64 v[48:49], v[48:49], v[10:11], s[52:53]
	v_fma_f64 v[48:49], v[48:49], v[10:11], s[54:55]
	v_fma_f64 v[48:49], v[48:49], v[10:11], s[56:57]
	v_fma_f64 v[48:49], v[48:49], v[10:11], s[58:59]
	v_fma_f64 v[48:49], v[48:49], v[10:11], s[60:61]
	v_fma_f64 v[48:49], v[48:49], v[10:11], 0.5
	v_fma_f64 v[48:49], v[48:49], v[10:11], 1.0
	v_fma_f64 v[48:49], v[48:49], v[10:11], 1.0
	v_cvt_i32_f64_e32 v50, v[46:47]
	v_ldexp_f64 v[48:49], v[48:49], v50
	v_fma_f64 v[48:49], v[6:7], v[48:49], -1.0
	v_add_f64 v[8:9], v[8:9], v[48:49]
	v_cvt_f64_f32_e32 v[10:11], v58
	s_mov_b32 s40, 0xfefa39ef
	s_mov_b32 s41, 0x3fe62e42
	v_fma_f64 v[8:9], -v[10:11], s[40:41], v[8:9]
	s_lshl_b32 s32, s24, 3
	s_lshl_b32 s33, s24, 2
	v_mov_b32_e32 v4, s28
	v_mov_b32_e32 v5, s29
	v_mov_b32_e32 v6, s30
	v_mov_b32_e32 v7, s31
	v_mov_b32_e32 v10, s32
	v_mov_b32_e32 v11, s33
	s_mov_b64 exec, 1
	global_store_dwordx2 v10, v[8:9], s[8:9]
	global_store_dword v11, v4, s[10:11]
	global_store_dword v11, v5, s[20:21]
	global_store_dword v11, v6, s[16:17]
	global_store_dword v11, v7, s[18:19]
	s_endpgm

_Z22k2_resolve_rank_gatherPKfS0_PKdS0_PKiPKyPKtS0_S4_Pf:
	s_load_dwordx16 s[4:19], s[0:1], 0x0
	s_load_dwordx4 s[20:23], s[0:1], 0x40
	v_and_b32_e32 v1, 0x3ff, v0
	s_lshr_b32 s24, s2, 6
	s_and_b32 s25, s2, 63
	s_lshl_b32 s26, s24, 9
	v_lshl_add_u32 v2, v1, 1, s26
	v_lshlrev_b32_e32 v3, 4, v2
	v_lshlrev_b32_e32 v24, 2, v2
	v_lshlrev_b32_e32 v25, 3, v2
	v_mov_b32_e32 v106, 0
	v_mov_b32_e32 v107, 0
	v_mov_b32_e32 v105, 0x1800
	v_lshlrev_b32_e32 v104, 3, v1
	s_movk_i32 s30, 0x641
	s_mov_b32 s32, 0xa0b5ed8d
	s_mov_b32 s33, 0x3ed0c6f7
	s_mov_b32 s34, 0xa0b5ed8d
	s_mov_b32 s35, 0xbed0c6f7
	s_mul_i32 s31, s26, 0x1904
	v_lshrrev_b32_e32 v29, 6, v1
	s_waitcnt lgkmcnt(0)
	global_load_dwordx4 v[4:7], v3, s[16:17]
	global_load_dwordx4 v[8:11], v3, s[16:17] offset:16
	global_load_dwordx2 v[12:13], v24, s[10:11]
	global_load_dwordx2 v[16:17], v24, s[12:13]
	global_load_dwordx4 v[20:23], v25, s[8:9]
	global_load_dwordx2 v[14:15], v24, s[18:19]
	global_load_dwordx2 v[18:19], v24, s[20:21]
	s_add_u32 s28, s4, s31
	s_addc_u32 s29, s5, 0
	v_readfirstlane_b32 s27, v29
	ds_write_b64 v105, v[106:107]
	ds_write_b64 v105, v[106:107] offset:8
	ds_write_b64 v105, v[106:107] offset:16
	ds_write_b64 v104, v[106:107] offset:8448
	s_mov_b64 s[36:37], 0
	s_mov_b64 s[38:39], 0
	s_mov_b64 s[40:41], 0
	s_mov_b64 s[42:43], 0
	s_mov_b64 s[44:45], 0
	v_lshlrev_b32_e32 v2, 4, v1
	s_waitcnt vmcnt(2)
	ds_write_b128 v2, v[20:23] offset:12544
	v_lshlrev_b32_e32 v3, 5, v1
	ds_write_b128 v3, v[4:7] offset:22784
	ds_write_b128 v3, v[8:11] offset:22800
	ds_write_b64 v104, v[16:17] offset:30976
	v_and_b32_e32 v26, 0xffff, v4
	v_and_b32_e32 v27, 0xffff, v8
	v_max_u32_e32 v28, v26, v27
	v_cvt_f64_f32_e32 v[92:93], v12
	v_cvt_f64_f32_e32 v[94:95], v13
	v_add_f64 v[92:93], v[92:93], -v[20:21]
	v_add_f64 v[94:95], v[94:95], -v[22:23]
	s_waitcnt vmcnt(0)
	ds_write_b64 v104, v[14:15] offset:33024
	v_cvt_f64_f32_e32 v[96:97], v14
	v_cvt_f64_f32_e32 v[98:99], v15
	v_add_f64 v[96:97], v[96:97], -v[20:21]
	v_add_f64 v[98:99], v[98:99], -v[22:23]
	v_cmp_lt_u32_e32 vcc, 0, v28
	s_cbranch_vccz .Lk2_l1a_done
	v_cmp_lt_u32_e32 vcc, 0, v26
	s_and_saveexec_b64 s[46:47], vcc
	s_cbranch_execz .Lk2_l1a_0_0
	v_lshrrev_b32_e32 v29, 16, v4
	v_mad_u32_u24 v30, v29, s30, v16
	v_mad_u32_u24 v31, v29, s30, v18
	v_lshlrev_b32_e32 v30, 2, v30
	v_lshlrev_b32_e32 v31, 2, v31
	global_load_dword v32, v30, s[28:29]
	global_load_dword v33, v31, s[28:29]
.Lk2_l1a_0_0:
	s_or_b64 exec, exec, s[46:47]
	v_cmp_lt_u32_e32 vcc, 0, v27
	s_and_saveexec_b64 s[46:47], vcc
	s_cbranch_execz .Lk2_l1a_0_1
	v_lshrrev_b32_e32 v29, 16, v8
	v_mad_u32_u24 v30, v29, s30, v17
	v_mad_u32_u24 v31, v29, s30, v19
	v_lshlrev_b32_e32 v30, 2, v30
	v_lshlrev_b32_e32 v31, 2, v31
	global_load_dword v36, v30, s[28:29]
	global_load_dword v37, v31, s[28:29]
.Lk2_l1a_0_1:
	s_or_b64 exec, exec, s[46:47]
	v_cmp_lt_u32_e32 vcc, 1, v28
	s_cbranch_vccz .Lk2_l1a_done
	v_cmp_lt_u32_e32 vcc, 1, v26
	s_and_saveexec_b64 s[46:47], vcc
	s_cbranch_execz .Lk2_l1a_1_0
	v_and_b32_e32 v29, 0xffff, v5
	v_mad_u32_u24 v30, v29, s30, v16
	v_mad_u32_u24 v31, v29, s30, v18
	v_lshlrev_b32_e32 v30, 2, v30
	v_lshlrev_b32_e32 v31, 2, v31
	global_load_dword v40, v30, s[28:29]
	global_load_dword v41, v31, s[28:29]
.Lk2_l1a_1_0:
	s_or_b64 exec, exec, s[46:47]
	v_cmp_lt_u32_e32 vcc, 1, v27
	s_and_saveexec_b64 s[46:47], vcc
	s_cbranch_execz .Lk2_l1a_1_1
	v_and_b32_e32 v29, 0xffff, v9
	v_mad_u32_u24 v30, v29, s30, v17
	v_mad_u32_u24 v31, v29, s30, v19
	v_lshlrev_b32_e32 v30, 2, v30
	v_lshlrev_b32_e32 v31, 2, v31
	global_load_dword v44, v30, s[28:29]
	global_load_dword v45, v31, s[28:29]
.Lk2_l1a_1_1:
	s_or_b64 exec, exec, s[46:47]
	v_cmp_lt_u32_e32 vcc, 2, v28
	s_cbranch_vccz .Lk2_l1a_done
	v_cmp_lt_u32_e32 vcc, 2, v26
	s_and_saveexec_b64 s[46:47], vcc
	s_cbranch_execz .Lk2_l1a_2_0
	v_lshrrev_b32_e32 v29, 16, v5
	v_mad_u32_u24 v30, v29, s30, v16
	v_mad_u32_u24 v31, v29, s30, v18
	v_lshlrev_b32_e32 v30, 2, v30
	v_lshlrev_b32_e32 v31, 2, v31
	global_load_dword v48, v30, s[28:29]
	global_load_dword v49, v31, s[28:29]
.Lk2_l1a_2_0:
	s_or_b64 exec, exec, s[46:47]
	v_cmp_lt_u32_e32 vcc, 2, v27
	s_and_saveexec_b64 s[46:47], vcc
	s_cbranch_execz .Lk2_l1a_2_1
	v_lshrrev_b32_e32 v29, 16, v9
	v_mad_u32_u24 v30, v29, s30, v17
	v_mad_u32_u24 v31, v29, s30, v19
	v_lshlrev_b32_e32 v30, 2, v30
	v_lshlrev_b32_e32 v31, 2, v31
	global_load_dword v52, v30, s[28:29]
	global_load_dword v53, v31, s[28:29]
.Lk2_l1a_2_1:
	s_or_b64 exec, exec, s[46:47]
	v_cmp_lt_u32_e32 vcc, 3, v28
	s_cbranch_vccz .Lk2_l1a_done
	v_cmp_lt_u32_e32 vcc, 3, v26
	s_and_saveexec_b64 s[46:47], vcc
	s_cbranch_execz .Lk2_l1a_3_0
	v_and_b32_e32 v29, 0xffff, v6
	v_mad_u32_u24 v30, v29, s30, v16
	v_mad_u32_u24 v31, v29, s30, v18
	v_lshlrev_b32_e32 v30, 2, v30
	v_lshlrev_b32_e32 v31, 2, v31
	global_load_dword v56, v30, s[28:29]
	global_load_dword v57, v31, s[28:29]
.Lk2_l1a_3_0:
	s_or_b64 exec, exec, s[46:47]
	v_cmp_lt_u32_e32 vcc, 3, v27
	s_and_saveexec_b64 s[46:47], vcc
	s_cbranch_execz .Lk2_l1a_3_1
	v_and_b32_e32 v29, 0xffff, v10
	v_mad_u32_u24 v30, v29, s30, v17
	v_mad_u32_u24 v31, v29, s30, v19
	v_lshlrev_b32_e32 v30, 2, v30
	v_lshlrev_b32_e32 v31, 2, v31
	global_load_dword v60, v30, s[28:29]
	global_load_dword v61, v31, s[28:29]
.Lk2_l1a_3_1:
	s_or_b64 exec, exec, s[46:47]
	v_cmp_lt_u32_e32 vcc, 4, v28
	s_cbranch_vccz .Lk2_l1a_done
	v_cmp_lt_u32_e32 vcc, 4, v26
	s_and_saveexec_b64 s[46:47], vcc
	s_cbranch_execz .Lk2_l1a_4_0
	v_lshrrev_b32_e32 v29, 16, v6
	v_mad_u32_u24 v30, v29, s30, v16
	v_mad_u32_u24 v31, v29, s30, v18
	v_lshlrev_b32_e32 v30, 2, v30
	v_lshlrev_b32_e32 v31, 2, v31
	global_load_dword v64, v30, s[28:29]
	global_load_dword v65, v31, s[28:29]
.Lk2_l1a_4_0:
	s_or_b64 exec, exec, s[46:47]
	v_cmp_lt_u32_e32 vcc, 4, v27
	s_and_saveexec_b64 s[46:47], vcc
	s_cbranch_execz .Lk2_l1a_4_1
	v_lshrrev_b32_e32 v29, 16, v10
	v_mad_u32_u24 v30, v29, s30, v17
	v_mad_u32_u24 v31, v29, s30, v19
	v_lshlrev_b32_e32 v30, 2, v30
	v_lshlrev_b32_e32 v31, 2, v31
	global_load_dword v68, v30, s[28:29]
	global_load_dword v69, v31, s[28:29]
.Lk2_l1a_4_1:
	s_or_b64 exec, exec, s[46:47]
	v_cmp_lt_u32_e32 vcc, 5, v28
	s_cbranch_vccz .Lk2_l1a_done
	v_cmp_lt_u32_e32 vcc, 5, v26
	s_and_saveexec_b64 s[46:47], vcc
	s_cbranch_execz .Lk2_l1a_5_0
	v_and_b32_e32 v29, 0xffff, v7
	v_mad_u32_u24 v30, v29, s30, v16
	v_mad_u32_u24 v31, v29, s30, v18
	v_lshlrev_b32_e32 v30, 2, v30
	v_lshlrev_b32_e32 v31, 2, v31
	global_load_dword v72, v30, s[28:29]
	global_load_dword v73, v31, s[28:29]
.Lk2_l1a_5_0:
	s_or_b64 exec, exec, s[46:47]
	v_cmp_lt_u32_e32 vcc, 5, v27
	s_and_saveexec_b64 s[46:47], vcc
	s_cbranch_execz .Lk2_l1a_5_1
	v_and_b32_e32 v29, 0xffff, v11
	v_mad_u32_u24 v30, v29, s30, v17
	v_mad_u32_u24 v31, v29, s30, v19
	v_lshlrev_b32_e32 v30, 2, v30
	v_lshlrev_b32_e32 v31, 2, v31
	global_load_dword v76, v30, s[28:29]
	global_load_dword v77, v31, s[28:29]
.Lk2_l1a_5_1:
	s_or_b64 exec, exec, s[46:47]
	v_cmp_lt_u32_e32 vcc, 6, v28
	s_cbranch_vccz .Lk2_l1a_done
	v_cmp_lt_u32_e32 vcc, 6, v26
	s_and_saveexec_b64 s[46:47], vcc
	s_cbranch_execz .Lk2_l1a_6_0
	v_lshrrev_b32_e32 v29, 16, v7
	v_mad_u32_u24 v30, v29, s30, v16
	v_mad_u32_u24 v31, v29, s30, v18
	v_lshlrev_b32_e32 v30, 2, v30
	v_lshlrev_b32_e32 v31, 2, v31
	global_load_dword v80, v30, s[28:29]
	global_load_dword v81, v31, s[28:29]
.Lk2_l1a_6_0:
	s_or_b64 exec, exec, s[46:47]
	v_cmp_lt_u32_e32 vcc, 6, v27
	s_and_saveexec_b64 s[46:47], vcc
	s_cbranch_execz .Lk2_l1a_6_1
	v_lshrrev_b32_e32 v29, 16, v11
	v_mad_u32_u24 v30, v29, s30, v17
	v_mad_u32_u24 v31, v29, s30, v19
	v_lshlrev_b32_e32 v30, 2, v30
	v_lshlrev_b32_e32 v31, 2, v31
	global_load_dword v84, v30, s[28:29]
	global_load_dword v85, v31, s[28:29]

.Lk2_l1a_done:
	s_waitcnt lgkmcnt(0)
	s_barrier
	v_cmp_lt_u32_e32 vcc, 0, v28
	s_cbranch_vccz .Lk2_l1_done
	v_cmp_lt_u32_e32 vcc, 0, v26
	s_and_saveexec_b64 s[46:47], vcc
	s_cbranch_execz .Lk2_l1_0_0
	v_lshrrev_b32_e32 v29, 16, v4
	v_lshlrev_b32_e32 v29, 3, v29
	ds_read_b64 v[34:35], v29 offset:12544
.Lk2_l1_0_0:
	s_or_b64 exec, exec, s[46:47]
	v_cmp_lt_u32_e32 vcc, 0, v27
	s_and_saveexec_b64 s[46:47], vcc
	s_cbranch_execz .Lk2_l1_0_1
	v_lshrrev_b32_e32 v29, 16, v8
	v_lshlrev_b32_e32 v29, 3, v29
	ds_read_b64 v[38:39], v29 offset:12544
.Lk2_l1_0_1:
	s_or_b64 exec, exec, s[46:47]
	v_cmp_lt_u32_e32 vcc, 1, v28
	s_cbranch_vccz .Lk2_l1_done
	v_cmp_lt_u32_e32 vcc, 1, v26
	s_and_saveexec_b64 s[46:47], vcc
	s_cbranch_execz .Lk2_l1_1_0
	v_and_b32_e32 v29, 0xffff, v5
	v_lshlrev_b32_e32 v29, 3, v29
	ds_read_b64 v[42:43], v29 offset:12544
.Lk2_l1_1_0:
	s_or_b64 exec, exec, s[46:47]
	v_cmp_lt_u32_e32 vcc, 1, v27
	s_and_saveexec_b64 s[46:47], vcc
	s_cbranch_execz .Lk2_l1_1_1
	v_and_b32_e32 v29, 0xffff, v9
	v_lshlrev_b32_e32 v29, 3, v29
	ds_read_b64 v[46:47], v29 offset:12544
.Lk2_l1_1_1:
	s_or_b64 exec, exec, s[46:47]
	v_cmp_lt_u32_e32 vcc, 2, v28
	s_cbranch_vccz .Lk2_l1_done
	v_cmp_lt_u32_e32 vcc, 2, v26
	s_and_saveexec_b64 s[46:47], vcc
	s_cbranch_execz .Lk2_l1_2_0
	v_lshrrev_b32_e32 v29, 16, v5
	v_lshlrev_b32_e32 v29, 3, v29
	ds_read_b64 v[50:51], v29 offset:12544
.Lk2_l1_2_0:
	s_or_b64 exec, exec, s[46:47]
	v_cmp_lt_u32_e32 vcc, 2, v27
	s_and_saveexec_b64 s[46:47], vcc
	s_cbranch_execz .Lk2_l1_2_1
	v_lshrrev_b32_e32 v29, 16, v9
	v_lshlrev_b32_e32 v29, 3, v29
	ds_read_b64 v[54:55], v29 offset:12544
.Lk2_l1_2_1:
	s_or_b64 exec, exec, s[46:47]
	v_cmp_lt_u32_e32 vcc, 3, v28
	s_cbranch_vccz .Lk2_l1_done
	v_cmp_lt_u32_e32 vcc, 3, v26
	s_and_saveexec_b64 s[46:47], vcc
	s_cbranch_execz .Lk2_l1_3_0
	v_and_b32_e32 v29, 0xffff, v6
	v_lshlrev_b32_e32 v29, 3, v29
	ds_read_b64 v[58:59], v29 offset:12544
.Lk2_l1_3_0:
	s_or_b64 exec, exec, s[46:47]
	v_cmp_lt_u32_e32 vcc, 3, v27
	s_and_saveexec_b64 s[46:47], vcc
	s_cbranch_execz .Lk2_l1_3_1
	v_and_b32_e32 v29, 0xffff, v10
	v_lshlrev_b32_e32 v29, 3, v29
	ds_read_b64 v[62:63], v29 offset:12544
.Lk2_l1_3_1:
	s_or_b64 exec, exec, s[46:47]
	v_cmp_lt_u32_e32 vcc, 4, v28
	s_cbranch_vccz .Lk2_l1_done
	v_cmp_lt_u32_e32 vcc, 4, v26
	s_and_saveexec_b64 s[46:47], vcc
	s_cbranch_execz .Lk2_l1_4_0
	v_lshrrev_b32_e32 v29, 16, v6
	v_lshlrev_b32_e32 v29, 3, v29
	ds_read_b64 v[66:67], v29 offset:12544
.Lk2_l1_4_0:
	s_or_b64 exec, exec, s[46:47]
	v_cmp_lt_u32_e32 vcc, 4, v27
	s_and_saveexec_b64 s[46:47], vcc
	s_cbranch_execz .Lk2_l1_4_1
	v_lshrrev_b32_e32 v29, 16, v10
	v_lshlrev_b32_e32 v29, 3, v29
	ds_read_b64 v[70:71], v29 offset:12544
.Lk2_l1_4_1:
	s_or_b64 exec, exec, s[46:47]
	v_cmp_lt_u32_e32 vcc, 5, v28
	s_cbranch_vccz .Lk2_l1_done
	v_cmp_lt_u32_e32 vcc, 5, v26
	s_and_saveexec_b64 s[46:47], vcc
	s_cbranch_execz .Lk2_l1_5_0
	v_and_b32_e32 v29, 0xffff, v7
	v_lshlrev_b32_e32 v29, 3, v29
	ds_read_b64 v[74:75], v29 offset:12544
.Lk2_l1_5_0:
	s_or_b64 exec, exec, s[46:47]
	v_cmp_lt_u32_e32 vcc, 5, v27
	s_and_saveexec_b64 s[46:47], vcc
	s_cbranch_execz .Lk2_l1_5_1
	v_and_b32_e32 v29, 0xffff, v11
	v_lshlrev_b32_e32 v29, 3, v29
	ds_read_b64 v[78:79], v29 offset:12544
.Lk2_l1_5_1:
	s_or_b64 exec, exec, s[46:47]
	v_cmp_lt_u32_e32 vcc, 6, v28
	s_cbranch_vccz .Lk2_l1_done
	v_cmp_lt_u32_e32 vcc, 6, v26
	s_and_saveexec_b64 s[46:47], vcc
	s_cbranch_execz .Lk2_l1_6_0
	v_lshrrev_b32_e32 v29, 16, v7
	v_lshlrev_b32_e32 v29, 3, v29
	ds_read_b64 v[82:83], v29 offset:12544
.Lk2_l1_6_0:
	s_or_b64 exec, exec, s[46:47]
	v_cmp_lt_u32_e32 vcc, 6, v27
	s_and_saveexec_b64 s[46:47], vcc
	s_cbranch_execz .Lk2_l1_6_1
	v_lshrrev_b32_e32 v29, 16, v11
	v_lshlrev_b32_e32 v29, 3, v29
	ds_read_b64 v[86:87], v29 offset:12544
